# v3 + pooling halo rows prefetched up front (prefix ladder no longer W serialized round trips)
# baseline (speedup 1.0000x reference)
; #define GAS __attribute__((address_space(1)))
; template <int W>
; __device__ __forceinline__ void pool_item(const bf16* U, bf16* Z, int b, int t0, int g, int lane) {
;     const size_t base = (size_t)b * SEQ * D + 256 * g + 4 * lane;
;     float s[4] = {0.f, 0.f, 0.f, 0.f};
; #pragma unroll
;     for (int j = 1; j <= W; ++j) { const int t = t0 - j; if (t >= 0) { const u32x2 v = *(const GAS u32x2*)(U + base + (size_t)t * D);
;             s[0] += bf2f(v.x & 0xffffu); s[1] += bf2f(v.x >> 16); s[2] += bf2f(v.y & 0xffffu); s[3] += bf2f(v.y >> 16); } }
.LBB0_869:
	s_nop 0
	v_writelane_b32 v255, s8, 3
	s_mov_b64 s[46:47], -1
	s_and_b64 vcc, exec, s[40:41]
	s_cbranch_vccz .LBB0_862
	v_readlane_b32 s8, v255, 4
	s_ashr_i32 s48, s8, 3
	s_lshl_b32 s8, s8, 8
	s_and_b32 s8, s8, 0x700
	s_ashr_i32 s49, s48, 31
	s_add_i32 s46, s8, s5
	s_lshl_b64 s[50:51], s[48:49], 21
	s_cmp_gt_i32 s46, 0
	v_readlane_b32 s9, v255, 3
	s_cselect_b64 s[40:41], -1, 0
	s_mov_b64 s[56:57], -1
	s_mov_b64 s[52:53], 0
	s_cmp_lt_i32 s9, 1
	s_mov_b64 s[54:55], 0
	s_cbranch_scc1 .LBB0_882
	v_readlane_b32 s9, v255, 3
	s_cmp_gt_i32 s9, 1
	s_cbranch_scc0 .LBB0_911
	s_cmp_eq_u32 s9, 2
	s_mov_b64 s[54:55], -1
	s_cbranch_scc0 .LBB0_910
	v_mov_b32_e32 v19, s51
	v_or_b32_e32 v18, s50, v6
	s_andn2_b64 vcc, exec, s[40:41]
	s_cbranch_vccnz .LBB0_1013
	s_add_i32 s22, s46, -2
	s_lshl_b64 s[10:11], s[22:23], 11
	s_add_u32 s10, s44, s10
	s_addc_u32 s11, s45, s11
	v_lshl_add_u64 v[20:21], v[18:19], 1, s[10:11]
	global_load_dwordx2 v[164:165], v[20:21], off
	s_add_i32 s22, s46, -3
	s_lshl_b64 s[10:11], s[22:23], 11
	s_add_u32 s10, s44, s10
	s_addc_u32 s11, s45, s11
	v_lshl_add_u64 v[20:21], v[18:19], 1, s[10:11]
	global_load_dwordx2 v[166:167], v[20:21], off
	s_add_i32 s22, s46, -4
	s_lshl_b64 s[10:11], s[22:23], 11
	s_add_u32 s10, s44, s10
	s_addc_u32 s11, s45, s11
	v_lshl_add_u64 v[20:21], v[18:19], 1, s[10:11]
	global_load_dwordx2 v[168:169], v[20:21], off
	s_add_i32 s22, s46, -5
	s_lshl_b64 s[10:11], s[22:23], 11
	s_add_u32 s10, s44, s10
	s_addc_u32 s11, s45, s11
	v_lshl_add_u64 v[20:21], v[18:19], 1, s[10:11]
	global_load_dwordx2 v[170:171], v[20:21], off
	s_add_i32 s22, s46, -6
	s_lshl_b64 s[10:11], s[22:23], 11
	s_add_u32 s10, s44, s10
	s_addc_u32 s11, s45, s11
	v_lshl_add_u64 v[20:21], v[18:19], 1, s[10:11]
	global_load_dwordx2 v[172:173], v[20:21], off
	s_add_i32 s22, s46, -7
	s_lshl_b64 s[10:11], s[22:23], 11
	s_add_u32 s10, s44, s10
	s_addc_u32 s11, s45, s11
	v_lshl_add_u64 v[20:21], v[18:19], 1, s[10:11]
	global_load_dwordx2 v[174:175], v[20:21], off
	s_add_i32 s22, s46, -8
	s_lshl_b64 s[10:11], s[22:23], 11
	s_add_u32 s10, s44, s10
	s_addc_u32 s11, s45, s11
	v_lshl_add_u64 v[20:21], v[18:19], 1, s[10:11]
	global_load_dwordx2 v[176:177], v[20:21], off
	s_add_i32 s22, s46, -1
	s_lshl_b64 s[10:11], s[22:23], 11
	s_add_u32 s10, s44, s10
	s_addc_u32 s11, s45, s11
	v_lshl_add_u64 v[20:21], v[18:19], 1, s[10:11]
	global_load_dwordx2 v[20:21], v[20:21], off
	s_waitcnt vmcnt(0)
	v_and_b32_e32 v22, 0xffff0000, v20
	v_lshlrev_b32_e32 v23, 16, v20
	v_and_b32_e32 v20, 0xffff0000, v21
	v_lshlrev_b32_e32 v21, 16, v21
	v_pk_add_f32 v[22:23], v[22:23], 0 op_sel_hi:[1,0]
	v_pk_add_f32 v[24:25], v[20:21], 0 op_sel_hi:[1,0]
	s_cmp_lt_i32 s46, 2
	s_cbranch_scc1 .LBB0_876

; #define GAS __attribute__((address_space(1)))
; template <int W>
; __device__ __forceinline__ void pool_item(const bf16* U, bf16* Z, int b, int t0, int g, int lane) {
;     const size_t base = (size_t)b * SEQ * D + 256 * g + 4 * lane;
;     float s[4] = {0.f, 0.f, 0.f, 0.f};
; #pragma unroll
;     for (int j = 1; j <= W; ++j) { const int t = t0 - j; if (t >= 0) { const u32x2 v = *(const GAS u32x2*)(U + base + (size_t)t * D);
;             s[0] += bf2f(v.x & 0xffffu); s[1] += bf2f(v.x >> 16); s[2] += bf2f(v.y & 0xffffu); s[3] += bf2f(v.y >> 16); } }
.LBB0_911:
	s_and_b64 vcc, exec, s[56:57]
	s_cbranch_vccz .LBB0_937
	v_mov_b32_e32 v19, s51
	v_or_b32_e32 v18, s50, v8
	s_andn2_b64 vcc, exec, s[40:41]
	s_cbranch_vccnz .LBB0_1012
	s_add_i32 s22, s46, -2
	s_lshl_b64 s[10:11], s[22:23], 11
	s_add_u32 s10, s44, s10
	s_addc_u32 s11, s45, s11
	v_lshl_add_u64 v[20:21], v[18:19], 1, s[10:11]
	global_load_dwordx2 v[164:165], v[20:21], off
	s_add_i32 s22, s46, -3
	s_lshl_b64 s[10:11], s[22:23], 11
	s_add_u32 s10, s44, s10
	s_addc_u32 s11, s45, s11
	v_lshl_add_u64 v[20:21], v[18:19], 1, s[10:11]
	global_load_dwordx2 v[166:167], v[20:21], off
	s_add_i32 s22, s46, -4
	s_lshl_b64 s[10:11], s[22:23], 11
	s_add_u32 s10, s44, s10
	s_addc_u32 s11, s45, s11
	v_lshl_add_u64 v[20:21], v[18:19], 1, s[10:11]
	global_load_dwordx2 v[168:169], v[20:21], off
	s_add_i32 s22, s46, -1
	s_lshl_b64 s[10:11], s[22:23], 11
	s_add_u32 s10, s44, s10
	s_addc_u32 s11, s45, s11
	v_lshl_add_u64 v[20:21], v[18:19], 1, s[10:11]
	global_load_dwordx2 v[20:21], v[20:21], off
	s_waitcnt vmcnt(0)
	v_lshlrev_b32_e32 v23, 16, v20
	v_and_b32_e32 v22, 0xffff0000, v20
	v_lshlrev_b32_e32 v25, 16, v21
	v_and_b32_e32 v24, 0xffff0000, v21
	v_pk_add_f32 v[28:29], v[22:23], 0 op_sel_hi:[1,0]
	v_pk_add_f32 v[30:31], v[24:25], 0 op_sel_hi:[1,0]
	s_cmp_lt_i32 s46, 2
	s_cbranch_scc1 .LBB0_915

; #define GAS __attribute__((address_space(1)))
; template <int W>
; __device__ __forceinline__ void pool_item(const bf16* U, bf16* Z, int b, int t0, int g, int lane) {
;     const size_t base = (size_t)b * SEQ * D + 256 * g + 4 * lane;
;     float s[4] = {0.f, 0.f, 0.f, 0.f};
; #pragma unroll
;     for (int j = 1; j <= W; ++j) { const int t = t0 - j; if (t >= 0) { const u32x2 v = *(const GAS u32x2*)(U + base + (size_t)t * D);
;             s[0] += bf2f(v.x & 0xffffu); s[1] += bf2f(v.x >> 16); s[2] += bf2f(v.y & 0xffffu); s[3] += bf2f(v.y >> 16); } }
.LBB0_939:
	v_mov_b32_e32 v19, s51
	s_and_b64 vcc, exec, s[40:41]
	v_or_b32_e32 v18, s50, v10
	s_cbranch_vccnz .LBB0_1010
	s_add_i32 s22, s46, -2
	s_lshl_b64 s[10:11], s[22:23], 11
	s_add_u32 s10, s44, s10
	s_addc_u32 s11, s45, s11
	v_lshl_add_u64 v[20:21], v[18:19], 1, s[10:11]
	global_load_dwordx2 v[164:165], v[20:21], off
	s_add_i32 s22, s46, -3
	s_lshl_b64 s[10:11], s[22:23], 11
	s_add_u32 s10, s44, s10
	s_addc_u32 s11, s45, s11
	v_lshl_add_u64 v[20:21], v[18:19], 1, s[10:11]
	global_load_dwordx2 v[166:167], v[20:21], off
	s_add_i32 s22, s46, -4
	s_lshl_b64 s[10:11], s[22:23], 11
	s_add_u32 s10, s44, s10
	s_addc_u32 s11, s45, s11
	v_lshl_add_u64 v[20:21], v[18:19], 1, s[10:11]
	global_load_dwordx2 v[168:169], v[20:21], off
	s_add_i32 s22, s46, -5
	s_lshl_b64 s[10:11], s[22:23], 11
	s_add_u32 s10, s44, s10
	s_addc_u32 s11, s45, s11
	v_lshl_add_u64 v[20:21], v[18:19], 1, s[10:11]
	global_load_dwordx2 v[170:171], v[20:21], off
	s_add_i32 s22, s46, -6
	s_lshl_b64 s[10:11], s[22:23], 11
	s_add_u32 s10, s44, s10
	s_addc_u32 s11, s45, s11
	v_lshl_add_u64 v[20:21], v[18:19], 1, s[10:11]
	global_load_dwordx2 v[172:173], v[20:21], off
	s_add_i32 s22, s46, -7
	s_lshl_b64 s[10:11], s[22:23], 11
	s_add_u32 s10, s44, s10
	s_addc_u32 s11, s45, s11
	v_lshl_add_u64 v[20:21], v[18:19], 1, s[10:11]
	global_load_dwordx2 v[174:175], v[20:21], off
	s_add_i32 s22, s46, -8
	s_lshl_b64 s[10:11], s[22:23], 11
	s_add_u32 s10, s44, s10
	s_addc_u32 s11, s45, s11
	v_lshl_add_u64 v[20:21], v[18:19], 1, s[10:11]
	global_load_dwordx2 v[176:177], v[20:21], off
	s_add_i32 s22, s46, -9
	s_lshl_b64 s[10:11], s[22:23], 11
	s_add_u32 s10, s44, s10
	s_addc_u32 s11, s45, s11
	v_lshl_add_u64 v[20:21], v[18:19], 1, s[10:11]
	global_load_dwordx2 v[178:179], v[20:21], off
	s_add_i32 s22, s46, -10
	s_lshl_b64 s[10:11], s[22:23], 11
	s_add_u32 s10, s44, s10
	s_addc_u32 s11, s45, s11
	v_lshl_add_u64 v[20:21], v[18:19], 1, s[10:11]
	global_load_dwordx2 v[180:181], v[20:21], off
	s_add_i32 s22, s46, -11
	s_lshl_b64 s[10:11], s[22:23], 11
	s_add_u32 s10, s44, s10
	s_addc_u32 s11, s45, s11
	v_lshl_add_u64 v[20:21], v[18:19], 1, s[10:11]
	global_load_dwordx2 v[182:183], v[20:21], off
	s_add_i32 s22, s46, -12
	s_lshl_b64 s[10:11], s[22:23], 11
	s_add_u32 s10, s44, s10
	s_addc_u32 s11, s45, s11
	v_lshl_add_u64 v[20:21], v[18:19], 1, s[10:11]
	global_load_dwordx2 v[184:185], v[20:21], off
	s_add_i32 s22, s46, -13
	s_lshl_b64 s[10:11], s[22:23], 11
	s_add_u32 s10, s44, s10
	s_addc_u32 s11, s45, s11
	v_lshl_add_u64 v[20:21], v[18:19], 1, s[10:11]
	global_load_dwordx2 v[186:187], v[20:21], off
	s_add_i32 s22, s46, -14
	s_lshl_b64 s[10:11], s[22:23], 11
	s_add_u32 s10, s44, s10
	s_addc_u32 s11, s45, s11
	v_lshl_add_u64 v[20:21], v[18:19], 1, s[10:11]
	global_load_dwordx2 v[188:189], v[20:21], off
	s_add_i32 s22, s46, -15
	s_lshl_b64 s[10:11], s[22:23], 11
	s_add_u32 s10, s44, s10
	s_addc_u32 s11, s45, s11
	v_lshl_add_u64 v[20:21], v[18:19], 1, s[10:11]
	global_load_dwordx2 v[190:191], v[20:21], off
	s_add_i32 s22, s46, -16
	s_lshl_b64 s[10:11], s[22:23], 11
	s_add_u32 s10, s44, s10
	s_addc_u32 s11, s45, s11
	v_lshl_add_u64 v[20:21], v[18:19], 1, s[10:11]
	global_load_dwordx2 v[192:193], v[20:21], off
	s_add_i32 s22, s46, -1
	s_lshl_b64 s[10:11], s[22:23], 11
	s_add_u32 s10, s44, s10
	s_addc_u32 s11, s45, s11
	v_lshl_add_u64 v[20:21], v[18:19], 1, s[10:11]
	global_load_dwordx2 v[20:21], v[20:21], off
	s_waitcnt vmcnt(0)
	v_lshlrev_b32_e32 v23, 16, v20
	v_and_b32_e32 v22, 0xffff0000, v20
	v_lshlrev_b32_e32 v25, 16, v21
	v_and_b32_e32 v24, 0xffff0000, v21
	v_pk_add_f32 v[22:23], v[22:23], 0 op_sel_hi:[1,0]
	v_pk_add_f32 v[24:25], v[24:25], 0 op_sel_hi:[1,0]
	s_cmp_lt_i32 s46, 2
	s_cbranch_scc1 .LBB0_942
